# window attention row sums also on VALU dot2c; score shift s-m packed two per instruction (v_pk_add_f32 with negated broadcast operand) in both attention kernels
# speedup vs baseline: 1.0059x; 1.0012x over previous
.LBB0_1569:
	v_pk_add_f32 v[130:131], v[130:131], v[66:67] op_sel_hi:[1,0] neg_lo:[0,1] neg_hi:[0,1]
	v_pk_add_f32 v[128:129], v[128:129], v[66:67] op_sel_hi:[1,0] neg_lo:[0,1] neg_hi:[0,1]
	v_pk_add_f32 v[126:127], v[126:127], v[66:67] op_sel_hi:[1,0] neg_lo:[0,1] neg_hi:[0,1]
	v_pk_add_f32 v[124:125], v[124:125], v[66:67] op_sel_hi:[1,0] neg_lo:[0,1] neg_hi:[0,1]
	v_pk_add_f32 v[122:123], v[122:123], v[66:67] op_sel_hi:[1,0] neg_lo:[0,1] neg_hi:[0,1]
	v_pk_add_f32 v[120:121], v[120:121], v[66:67] op_sel_hi:[1,0] neg_lo:[0,1] neg_hi:[0,1]
	v_pk_add_f32 v[118:119], v[118:119], v[66:67] op_sel_hi:[1,0] neg_lo:[0,1] neg_hi:[0,1]
	v_pk_add_f32 v[116:117], v[116:117], v[66:67] op_sel_hi:[1,0] neg_lo:[0,1] neg_hi:[0,1]
	v_pk_add_f32 v[146:147], v[146:147], v[66:67] op_sel_hi:[1,0] neg_lo:[0,1] neg_hi:[0,1]
	v_pk_add_f32 v[144:145], v[144:145], v[66:67] op_sel_hi:[1,0] neg_lo:[0,1] neg_hi:[0,1]
	v_pk_add_f32 v[142:143], v[142:143], v[66:67] op_sel_hi:[1,0] neg_lo:[0,1] neg_hi:[0,1]
	v_pk_add_f32 v[140:141], v[140:141], v[66:67] op_sel_hi:[1,0] neg_lo:[0,1] neg_hi:[0,1]
	v_pk_add_f32 v[138:139], v[138:139], v[66:67] op_sel_hi:[1,0] neg_lo:[0,1] neg_hi:[0,1]
	v_pk_add_f32 v[136:137], v[136:137], v[66:67] op_sel_hi:[1,0] neg_lo:[0,1] neg_hi:[0,1]
	v_pk_add_f32 v[134:135], v[134:135], v[66:67] op_sel_hi:[1,0] neg_lo:[0,1] neg_hi:[0,1]
	v_pk_add_f32 v[132:133], v[132:133], v[66:67] op_sel_hi:[1,0] neg_lo:[0,1] neg_hi:[0,1]

.LBB0_1600:
	v_cmp_neq_f32_e32 vcc, 0, v66
	s_cbranch_vccz .LBB0_1602
	v_pk_add_f32 v[50:51], v[50:51], v[66:67] op_sel_hi:[1,0] neg_lo:[0,1] neg_hi:[0,1]
	v_pk_add_f32 v[48:49], v[48:49], v[66:67] op_sel_hi:[1,0] neg_lo:[0,1] neg_hi:[0,1]
	v_pk_add_f32 v[46:47], v[46:47], v[66:67] op_sel_hi:[1,0] neg_lo:[0,1] neg_hi:[0,1]
	v_pk_add_f32 v[44:45], v[44:45], v[66:67] op_sel_hi:[1,0] neg_lo:[0,1] neg_hi:[0,1]
	v_pk_add_f32 v[42:43], v[42:43], v[66:67] op_sel_hi:[1,0] neg_lo:[0,1] neg_hi:[0,1]
	v_pk_add_f32 v[40:41], v[40:41], v[66:67] op_sel_hi:[1,0] neg_lo:[0,1] neg_hi:[0,1]
	v_pk_add_f32 v[38:39], v[38:39], v[66:67] op_sel_hi:[1,0] neg_lo:[0,1] neg_hi:[0,1]
	v_pk_add_f32 v[36:37], v[36:37], v[66:67] op_sel_hi:[1,0] neg_lo:[0,1] neg_hi:[0,1]
	v_pk_add_f32 v[82:83], v[82:83], v[66:67] op_sel_hi:[1,0] neg_lo:[0,1] neg_hi:[0,1]
	v_pk_add_f32 v[80:81], v[80:81], v[66:67] op_sel_hi:[1,0] neg_lo:[0,1] neg_hi:[0,1]
	v_pk_add_f32 v[78:79], v[78:79], v[66:67] op_sel_hi:[1,0] neg_lo:[0,1] neg_hi:[0,1]
	v_pk_add_f32 v[76:77], v[76:77], v[66:67] op_sel_hi:[1,0] neg_lo:[0,1] neg_hi:[0,1]
	v_pk_add_f32 v[74:75], v[74:75], v[66:67] op_sel_hi:[1,0] neg_lo:[0,1] neg_hi:[0,1]
	v_pk_add_f32 v[72:73], v[72:73], v[66:67] op_sel_hi:[1,0] neg_lo:[0,1] neg_hi:[0,1]
	v_pk_add_f32 v[70:71], v[70:71], v[66:67] op_sel_hi:[1,0] neg_lo:[0,1] neg_hi:[0,1]
	v_pk_add_f32 v[68:69], v[68:69], v[66:67] op_sel_hi:[1,0] neg_lo:[0,1] neg_hi:[0,1]

.LBB0_1633:
	v_cmp_neq_f32_e32 vcc, 0, v66
	s_cbranch_vccz .LBB0_1635
	v_pk_add_f32 v[130:131], v[130:131], v[66:67] op_sel_hi:[1,0] neg_lo:[0,1] neg_hi:[0,1]
	v_pk_add_f32 v[128:129], v[128:129], v[66:67] op_sel_hi:[1,0] neg_lo:[0,1] neg_hi:[0,1]
	v_pk_add_f32 v[126:127], v[126:127], v[66:67] op_sel_hi:[1,0] neg_lo:[0,1] neg_hi:[0,1]
	v_pk_add_f32 v[124:125], v[124:125], v[66:67] op_sel_hi:[1,0] neg_lo:[0,1] neg_hi:[0,1]
	v_pk_add_f32 v[122:123], v[122:123], v[66:67] op_sel_hi:[1,0] neg_lo:[0,1] neg_hi:[0,1]
	v_pk_add_f32 v[120:121], v[120:121], v[66:67] op_sel_hi:[1,0] neg_lo:[0,1] neg_hi:[0,1]
	v_pk_add_f32 v[118:119], v[118:119], v[66:67] op_sel_hi:[1,0] neg_lo:[0,1] neg_hi:[0,1]
	v_pk_add_f32 v[116:117], v[116:117], v[66:67] op_sel_hi:[1,0] neg_lo:[0,1] neg_hi:[0,1]
	v_pk_add_f32 v[146:147], v[146:147], v[66:67] op_sel_hi:[1,0] neg_lo:[0,1] neg_hi:[0,1]
	v_pk_add_f32 v[144:145], v[144:145], v[66:67] op_sel_hi:[1,0] neg_lo:[0,1] neg_hi:[0,1]
	v_pk_add_f32 v[142:143], v[142:143], v[66:67] op_sel_hi:[1,0] neg_lo:[0,1] neg_hi:[0,1]
	v_pk_add_f32 v[140:141], v[140:141], v[66:67] op_sel_hi:[1,0] neg_lo:[0,1] neg_hi:[0,1]
	v_pk_add_f32 v[138:139], v[138:139], v[66:67] op_sel_hi:[1,0] neg_lo:[0,1] neg_hi:[0,1]
	v_pk_add_f32 v[136:137], v[136:137], v[66:67] op_sel_hi:[1,0] neg_lo:[0,1] neg_hi:[0,1]
	v_pk_add_f32 v[134:135], v[134:135], v[66:67] op_sel_hi:[1,0] neg_lo:[0,1] neg_hi:[0,1]
	v_pk_add_f32 v[132:133], v[132:133], v[66:67] op_sel_hi:[1,0] neg_lo:[0,1] neg_hi:[0,1]

.LBB0_1932:
	v_exp_f32_e32 v50, v50
	v_exp_f32_e32 v66, v66
	v_exp_f32_e32 v51, v51
	v_exp_f32_e32 v67, v67
	v_exp_f32_e32 v52, v52
	v_exp_f32_e32 v68, v68
	v_exp_f32_e32 v53, v53
	v_exp_f32_e32 v69, v69
	v_exp_f32_e32 v54, v54
	v_exp_f32_e32 v70, v70
	v_exp_f32_e32 v55, v55
	v_exp_f32_e32 v71, v71
	v_exp_f32_e32 v56, v56
	v_exp_f32_e32 v72, v72
	v_exp_f32_e32 v57, v57
	v_exp_f32_e32 v73, v73
	v_exp_f32_e32 v58, v58
	v_exp_f32_e32 v74, v74
	v_exp_f32_e32 v59, v59
	v_exp_f32_e32 v75, v75
	v_exp_f32_e32 v60, v60
	v_exp_f32_e32 v76, v76
	v_exp_f32_e32 v61, v61
	v_exp_f32_e32 v77, v77
	v_exp_f32_e32 v62, v62
	v_exp_f32_e32 v78, v78
	v_exp_f32_e32 v63, v63
	v_exp_f32_e32 v79, v79
	v_exp_f32_e32 v64, v64
	v_exp_f32_e32 v80, v80
	v_exp_f32_e32 v65, v65
	v_exp_f32_e32 v81, v81
	v_cvt_pk_bf16_f32 v50, v50, v51
	v_cvt_pk_bf16_f32 v51, v52, v53
	v_cvt_pk_bf16_f32 v52, v54, v55
	v_cvt_pk_bf16_f32 v53, v56, v57
	v_cvt_pk_bf16_f32 v54, v66, v67
	v_cvt_pk_bf16_f32 v55, v68, v69
	v_cvt_pk_bf16_f32 v56, v70, v71
	v_cvt_pk_bf16_f32 v57, v72, v73
	v_cvt_pk_bf16_f32 v58, v58, v59
	v_cvt_pk_bf16_f32 v59, v60, v61
	v_cvt_pk_bf16_f32 v60, v62, v63
	v_cvt_pk_bf16_f32 v61, v64, v65
	v_cvt_pk_bf16_f32 v62, v74, v75
	v_cvt_pk_bf16_f32 v63, v76, v77
	v_cvt_pk_bf16_f32 v64, v78, v79
	v_cvt_pk_bf16_f32 v65, v80, v81
	v_mov_b64_e32 v[66:67], s[92:93]
	v_mov_b64_e32 v[68:69], s[94:95]
	s_not_b32 s2, s85
	s_lshl_b32 s2, s2, 13
	s_and_b32 s2, s2, 0x2000
	s_add_i32 s2, s2, 0
	v_dot2c_f32_bf16 v34, 0x3f803f80, v50
	v_dot2c_f32_bf16 v35, 0x3f803f80, v51
	v_dot2c_f32_bf16 v34, 0x3f803f80, v52
	v_dot2c_f32_bf16 v35, 0x3f803f80, v53
	s_addk_i32 s2, 0x4000
	v_add_u32_e32 v82, s2, v177
	v_add_u32_e32 v83, s2, v178
	ds_read_b64_tr_b16 v[70:71], v82 offset:0
	ds_read_b64_tr_b16 v[72:73], v82 offset:1024
	ds_read_b64_tr_b16 v[74:75], v83 offset:0
	ds_read_b64_tr_b16 v[76:77], v83 offset:1024
	v_dot2c_f32_bf16 v34, 0x3f803f80, v58
	v_dot2c_f32_bf16 v35, 0x3f803f80, v59
	v_dot2c_f32_bf16 v34, 0x3f803f80, v60
	v_dot2c_f32_bf16 v35, 0x3f803f80, v61
	v_dot2c_f32_bf16 v34, 0x3f803f80, v54
	v_dot2c_f32_bf16 v35, 0x3f803f80, v55
	v_dot2c_f32_bf16 v34, 0x3f803f80, v56
	v_dot2c_f32_bf16 v35, 0x3f803f80, v57
	v_dot2c_f32_bf16 v34, 0x3f803f80, v62
	v_dot2c_f32_bf16 v35, 0x3f803f80, v63
	v_dot2c_f32_bf16 v34, 0x3f803f80, v64
	v_dot2c_f32_bf16 v35, 0x3f803f80, v65
	ds_read_b64_tr_b16 v[66:67], v82 offset:2048
	ds_read_b64_tr_b16 v[68:69], v82 offset:3072
	ds_read_b64_tr_b16 v[78:79], v83 offset:2048
	ds_read_b64_tr_b16 v[80:81], v83 offset:3072
	s_nop 0
	s_waitcnt lgkmcnt(0)
	ds_read_b64_tr_b16 v[36:37], v82 offset:4096
	ds_read_b64_tr_b16 v[38:39], v82 offset:5120
	ds_read_b64_tr_b16 v[40:41], v83 offset:4096
	ds_read_b64_tr_b16 v[42:43], v83 offset:5120
	ds_read_b64_tr_b16 v[44:45], v82 offset:6144
	s_nop 0
	v_mfma_f32_32x32x16_bf16 v[18:33], v[70:73], v[50:53], v[18:33]
	ds_read_b64_tr_b16 v[46:47], v82 offset:7168
	ds_read_b64_tr_b16 v[48:49], v83 offset:6144
	v_mfma_f32_32x32x16_bf16 v[2:17], v[74:77], v[50:53], v[2:17]
	ds_read_b64_tr_b16 v[50:51], v83 offset:7168
	s_nop 0
	s_waitcnt lgkmcnt(0)
	v_mfma_f32_32x32x16_bf16 v[18:33], v[66:69], v[58:61], v[18:33]
	v_mfma_f32_32x32x16_bf16 v[2:17], v[78:81], v[58:61], v[2:17]
	s_nop 4
	v_mfma_f32_32x32x16_bf16 v[18:33], v[36:39], v[54:57], v[18:33]
	v_mfma_f32_32x32x16_bf16 v[2:17], v[40:43], v[54:57], v[2:17]
	v_mfma_f32_32x32x16_bf16 v[18:33], v[44:47], v[62:65], v[18:33]
	v_mfma_f32_32x32x16_bf16 v[2:17], v[48:51], v[62:65], v[2:17]
	s_setprio 0
	v_add_f32_e32 v36, v34, v35
	v_mov_b32_e32 v37, v36
	s_nop 1
	v_permlane32_swap_b32_e32 v36, v37
	v_add_f32_e32 v37, v36, v37
	v_fmac_f32_e32 v175, 0.5, v37
	v_mov_b32_e32 v36, v175
	v_readlane_b32 s2, v255, 30
	s_nop 0
	v_permlane32_swap_b32_e32 v175, v36
	v_lshlrev_b64 v[34:35], 11, v[144:145]
	v_readlane_b32 s3, v255, 31
	v_add_f32_e32 v36, v175, v175
	v_lshlrev_b32_e32 v98, 1, v116
	v_lshl_add_u64 v[34:35], s[2:3], 0, v[34:35]
	v_div_scale_f32 v37, s[2:3], v36, v36, 1.0
	v_rcp_f32_e32 v38, v37
	v_lshl_add_u64 v[34:35], v[146:147], 1, v[34:35]
	v_lshl_add_u64 v[34:35], v[34:35], 0, v[98:99]
	s_addk_i32 s84, 0x100
	v_fma_f32 v39, -v37, v38, 1.0
	v_fmac_f32_e32 v38, v39, v38
	v_div_scale_f32 v39, vcc, 1.0, v36, 1.0
	v_mul_f32_e32 v40, v39, v38
	v_fma_f32 v41, -v37, v40, v39
	v_fmac_f32_e32 v40, v41, v38
	v_fma_f32 v37, -v37, v40, v39
	v_div_fmas_f32 v37, v37, v38, v40
	v_div_fixup_f32 v36, v37, v36, 1.0
	v_pk_mul_f32 v[18:19], v[18:19], v[36:37] op_sel_hi:[1,0]
	v_pk_mul_f32 v[20:21], v[20:21], v[36:37] op_sel_hi:[1,0]
	v_pk_mul_f32 v[2:3], v[2:3], v[36:37] op_sel_hi:[1,0]
	v_pk_mul_f32 v[4:5], v[4:5], v[36:37] op_sel_hi:[1,0]
	v_cvt_pk_bf16_f32 v18, v18, v19
	v_cvt_pk_bf16_f32 v19, v20, v21
	v_pk_mul_f32 v[20:21], v[22:23], v[36:37] op_sel_hi:[1,0]
	v_pk_mul_f32 v[22:23], v[24:25], v[36:37] op_sel_hi:[1,0]
	v_cvt_pk_bf16_f32 v2, v2, v3
	v_cvt_pk_bf16_f32 v3, v4, v5
	v_pk_mul_f32 v[4:5], v[6:7], v[36:37] op_sel_hi:[1,0]
	v_pk_mul_f32 v[6:7], v[8:9], v[36:37] op_sel_hi:[1,0]
	v_cvt_pk_bf16_f32 v20, v20, v21
	v_cvt_pk_bf16_f32 v21, v22, v23
	v_cvt_pk_bf16_f32 v4, v4, v5
	v_cvt_pk_bf16_f32 v5, v6, v7
	v_permlane32_swap_b32_e32 v18, v20
	v_permlane32_swap_b32_e32 v19, v21
	v_permlane32_swap_b32_e32 v2, v4
	v_permlane32_swap_b32_e32 v3, v5
	global_store_dwordx4 v[34:35], v[18:21], off
	global_store_dwordx4 v[34:35], v[2:5], off offset:64
	v_pk_mul_f32 v[22:23], v[32:33], v[36:37] op_sel_hi:[1,0]
	v_pk_mul_f32 v[18:19], v[26:27], v[36:37] op_sel_hi:[1,0]
	v_pk_mul_f32 v[20:21], v[28:29], v[36:37] op_sel_hi:[1,0]
	v_pk_mul_f32 v[2:3], v[10:11], v[36:37] op_sel_hi:[1,0]
	v_pk_mul_f32 v[4:5], v[12:13], v[36:37] op_sel_hi:[1,0]
	v_cvt_pk_bf16_f32 v18, v18, v19
	v_cvt_pk_bf16_f32 v19, v20, v21
	v_pk_mul_f32 v[20:21], v[30:31], v[36:37] op_sel_hi:[1,0]
	v_cvt_pk_bf16_f32 v2, v2, v3
	v_cvt_pk_bf16_f32 v3, v4, v5
	v_pk_mul_f32 v[4:5], v[14:15], v[36:37] op_sel_hi:[1,0]
	v_pk_mul_f32 v[6:7], v[16:17], v[36:37] op_sel_hi:[1,0]
	v_cvt_pk_bf16_f32 v20, v20, v21
	v_cvt_pk_bf16_f32 v21, v22, v23
	v_cvt_pk_bf16_f32 v4, v4, v5
	v_cvt_pk_bf16_f32 v5, v6, v7
	v_permlane32_swap_b32_e32 v18, v20
	v_permlane32_swap_b32_e32 v19, v21
	v_permlane32_swap_b32_e32 v2, v4
	v_permlane32_swap_b32_e32 v3, v5
	s_cmp_ge_u32 s84, s82
	global_store_dwordx4 v[34:35], v[18:21], off offset:32
	global_store_dwordx4 v[34:35], v[2:5], off offset:96
	s_cbranch_scc1 .LBB0_2100

.LBB0_1973:
	v_pk_add_f32 v[64:65], v[64:65], v[184:185] op_sel_hi:[1,0] neg_lo:[0,1] neg_hi:[0,1]
	v_pk_add_f32 v[62:63], v[62:63], v[184:185] op_sel_hi:[1,0] neg_lo:[0,1] neg_hi:[0,1]
	v_pk_add_f32 v[60:61], v[60:61], v[184:185] op_sel_hi:[1,0] neg_lo:[0,1] neg_hi:[0,1]
	v_pk_add_f32 v[58:59], v[58:59], v[184:185] op_sel_hi:[1,0] neg_lo:[0,1] neg_hi:[0,1]
	v_pk_add_f32 v[56:57], v[56:57], v[184:185] op_sel_hi:[1,0] neg_lo:[0,1] neg_hi:[0,1]
	v_pk_add_f32 v[54:55], v[54:55], v[184:185] op_sel_hi:[1,0] neg_lo:[0,1] neg_hi:[0,1]
	v_pk_add_f32 v[52:53], v[52:53], v[184:185] op_sel_hi:[1,0] neg_lo:[0,1] neg_hi:[0,1]
	v_pk_add_f32 v[50:51], v[50:51], v[184:185] op_sel_hi:[1,0] neg_lo:[0,1] neg_hi:[0,1]
	v_pk_add_f32 v[80:81], v[80:81], v[184:185] op_sel_hi:[1,0] neg_lo:[0,1] neg_hi:[0,1]
	v_pk_add_f32 v[78:79], v[78:79], v[184:185] op_sel_hi:[1,0] neg_lo:[0,1] neg_hi:[0,1]
	v_pk_add_f32 v[76:77], v[76:77], v[184:185] op_sel_hi:[1,0] neg_lo:[0,1] neg_hi:[0,1]
	v_pk_add_f32 v[74:75], v[74:75], v[184:185] op_sel_hi:[1,0] neg_lo:[0,1] neg_hi:[0,1]
	v_pk_add_f32 v[72:73], v[72:73], v[184:185] op_sel_hi:[1,0] neg_lo:[0,1] neg_hi:[0,1]
	v_pk_add_f32 v[70:71], v[70:71], v[184:185] op_sel_hi:[1,0] neg_lo:[0,1] neg_hi:[0,1]
	v_pk_add_f32 v[68:69], v[68:69], v[184:185] op_sel_hi:[1,0] neg_lo:[0,1] neg_hi:[0,1]
	v_pk_add_f32 v[66:67], v[66:67], v[184:185] op_sel_hi:[1,0] neg_lo:[0,1] neg_hi:[0,1]

.LBB0_2006:
	v_max3_f32 v86, v100, v101, v116
	v_max_f32_e32 v87, v115, v115
	v_max3_f32 v86, v86, v117, v102
	s_nop 0
	v_dot2c_f32_bf16 v34, 0x3f803f80, v58
	v_dot2c_f32_bf16 v35, 0x3f803f80, v59
	v_dot2c_f32_bf16 v34, 0x3f803f80, v60
	v_dot2c_f32_bf16 v35, 0x3f803f80, v61
	v_max3_f32 v86, v86, v118, v119
	v_max3_f32 v86, v86, v103, v104
	v_max3_f32 v86, v86, v120, v121
	v_max3_f32 v86, v86, v105, v106
	v_dot2c_f32_bf16 v34, 0x3f803f80, v62
	v_dot2c_f32_bf16 v35, 0x3f803f80, v63
	v_dot2c_f32_bf16 v34, 0x3f803f80, v64
	v_dot2c_f32_bf16 v35, 0x3f803f80, v65
	v_max3_f32 v86, v86, v122, v123
	v_max3_f32 v86, v86, v107, v108
	v_max3_f32 v86, v86, v124, v125
	v_max3_f32 v86, v86, v109, v110
	v_dot2c_f32_bf16 v34, 0x3f803f80, v54
	v_dot2c_f32_bf16 v35, 0x3f803f80, v55
	v_dot2c_f32_bf16 v34, 0x3f803f80, v56
	v_dot2c_f32_bf16 v35, 0x3f803f80, v57
	v_max3_f32 v86, v86, v126, v127
	v_max3_f32 v86, v86, v111, v112
	v_max3_f32 v86, v86, v128, v129
	v_max3_f32 v86, v86, v113, v114
	v_dot2c_f32_bf16 v34, 0x3f803f80, v50
	v_dot2c_f32_bf16 v35, 0x3f803f80, v51
	v_dot2c_f32_bf16 v34, 0x3f803f80, v52
	v_dot2c_f32_bf16 v35, 0x3f803f80, v53
	v_max3_f32 v86, v86, v130, v131
	v_max_f32_e32 v86, v86, v86
	v_max_f32_e32 v86, v86, v87
	v_mov_b32_e32 v87, v86
	s_nop 1
	v_permlane32_swap_b32_e32 v86, v87
	v_sub_f32_e32 v86, v86, v184
	s_waitcnt lgkmcnt(0)
	s_nop 0
	v_mfma_f32_32x32x16_bf16 v[18:33], v[78:81], v[58:61], v[18:33]
	v_mfma_f32_32x32x16_bf16 v[2:17], v[74:77], v[58:61], v[2:17]
	ds_read_b64_tr_b16 v[58:59], v200 offset:4096
	ds_read_b64_tr_b16 v[60:61], v200 offset:5120
	v_mfma_f32_32x32x16_bf16 v[18:33], v[70:73], v[62:65], v[18:33]
	v_mfma_f32_32x32x16_bf16 v[2:17], v[66:69], v[62:65], v[2:17]
	ds_read_b64_tr_b16 v[62:63], v201 offset:4096
	ds_read_b64_tr_b16 v[64:65], v201 offset:5120
	ds_read_b64_tr_b16 v[66:67], v200 offset:6144
	ds_read_b64_tr_b16 v[68:69], v200 offset:7168
	ds_read_b64_tr_b16 v[70:71], v201 offset:6144
	ds_read_b64_tr_b16 v[72:73], v201 offset:7168
	s_nop 0
	s_waitcnt lgkmcnt(0)
	s_nop 0
	v_mfma_f32_32x32x16_bf16 v[18:33], v[58:61], v[54:57], v[18:33]
	v_mfma_f32_32x32x16_bf16 v[2:17], v[62:65], v[54:57], v[2:17]
	v_mfma_f32_32x32x16_bf16 v[18:33], v[66:69], v[50:53], v[18:33]
	v_mfma_f32_32x32x16_bf16 v[2:17], v[70:73], v[50:53], v[2:17]
	v_cmp_lt_f32_e32 vcc, s29, v86
	s_cbranch_vccz .LBB0_2008
	v_max_f32_e32 v50, v86, v86
	v_max_f32_e32 v51, 0, v50
	v_exp_f32_e64 v50, -v51
	v_add_f32_e32 v184, v184, v51
	v_mul_f32_e32 v175, v175, v50
	v_pk_mul_f32 v[48:49], v[48:49], v[50:51] op_sel_hi:[1,0]
	v_pk_mul_f32 v[46:47], v[46:47], v[50:51] op_sel_hi:[1,0]
	v_pk_mul_f32 v[44:45], v[44:45], v[50:51] op_sel_hi:[1,0]
	v_pk_mul_f32 v[42:43], v[42:43], v[50:51] op_sel_hi:[1,0]
	v_pk_mul_f32 v[40:41], v[40:41], v[50:51] op_sel_hi:[1,0]
	v_pk_mul_f32 v[38:39], v[38:39], v[50:51] op_sel_hi:[1,0]
	v_pk_mul_f32 v[36:37], v[36:37], v[50:51] op_sel_hi:[1,0]
	v_pk_mul_f32 v[34:35], v[34:35], v[50:51] op_sel_hi:[1,0]
	v_pk_mul_f32 v[16:17], v[50:51], v[16:17] op_sel_hi:[0,1]
	v_pk_mul_f32 v[14:15], v[50:51], v[14:15] op_sel_hi:[0,1]
	v_pk_mul_f32 v[12:13], v[50:51], v[12:13] op_sel_hi:[0,1]
	v_pk_mul_f32 v[10:11], v[50:51], v[10:11] op_sel_hi:[0,1]
	v_pk_mul_f32 v[8:9], v[50:51], v[8:9] op_sel_hi:[0,1]
	v_pk_mul_f32 v[6:7], v[50:51], v[6:7] op_sel_hi:[0,1]
	v_pk_mul_f32 v[4:5], v[50:51], v[4:5] op_sel_hi:[0,1]
	v_pk_mul_f32 v[2:3], v[50:51], v[2:3] op_sel_hi:[0,1]
	v_pk_mul_f32 v[32:33], v[50:51], v[32:33] op_sel_hi:[0,1]
	v_pk_mul_f32 v[30:31], v[50:51], v[30:31] op_sel_hi:[0,1]
	v_pk_mul_f32 v[28:29], v[50:51], v[28:29] op_sel_hi:[0,1]
	v_pk_mul_f32 v[26:27], v[50:51], v[26:27] op_sel_hi:[0,1]
	v_pk_mul_f32 v[24:25], v[50:51], v[24:25] op_sel_hi:[0,1]
	v_pk_mul_f32 v[22:23], v[50:51], v[22:23] op_sel_hi:[0,1]
	v_pk_mul_f32 v[20:21], v[50:51], v[20:21] op_sel_hi:[0,1]
	v_pk_mul_f32 v[18:19], v[50:51], v[18:19] op_sel_hi:[0,1]
.LBB0_2008:
	v_cmp_neq_f32_e32 vcc, 0, v184
	s_cbranch_vccz .LBB0_2010
	v_pk_add_f32 v[114:115], v[114:115], v[184:185] op_sel_hi:[1,0] neg_lo:[0,1] neg_hi:[0,1]
	v_pk_add_f32 v[112:113], v[112:113], v[184:185] op_sel_hi:[1,0] neg_lo:[0,1] neg_hi:[0,1]
	v_pk_add_f32 v[110:111], v[110:111], v[184:185] op_sel_hi:[1,0] neg_lo:[0,1] neg_hi:[0,1]
	v_pk_add_f32 v[108:109], v[108:109], v[184:185] op_sel_hi:[1,0] neg_lo:[0,1] neg_hi:[0,1]
	v_pk_add_f32 v[106:107], v[106:107], v[184:185] op_sel_hi:[1,0] neg_lo:[0,1] neg_hi:[0,1]
	v_pk_add_f32 v[104:105], v[104:105], v[184:185] op_sel_hi:[1,0] neg_lo:[0,1] neg_hi:[0,1]
	v_pk_add_f32 v[102:103], v[102:103], v[184:185] op_sel_hi:[1,0] neg_lo:[0,1] neg_hi:[0,1]
	v_pk_add_f32 v[100:101], v[100:101], v[184:185] op_sel_hi:[1,0] neg_lo:[0,1] neg_hi:[0,1]
	v_pk_add_f32 v[130:131], v[130:131], v[184:185] op_sel_hi:[1,0] neg_lo:[0,1] neg_hi:[0,1]
	v_pk_add_f32 v[128:129], v[128:129], v[184:185] op_sel_hi:[1,0] neg_lo:[0,1] neg_hi:[0,1]
	v_pk_add_f32 v[126:127], v[126:127], v[184:185] op_sel_hi:[1,0] neg_lo:[0,1] neg_hi:[0,1]
	v_pk_add_f32 v[124:125], v[124:125], v[184:185] op_sel_hi:[1,0] neg_lo:[0,1] neg_hi:[0,1]
	v_pk_add_f32 v[122:123], v[122:123], v[184:185] op_sel_hi:[1,0] neg_lo:[0,1] neg_hi:[0,1]
	v_pk_add_f32 v[120:121], v[120:121], v[184:185] op_sel_hi:[1,0] neg_lo:[0,1] neg_hi:[0,1]
	v_pk_add_f32 v[118:119], v[118:119], v[184:185] op_sel_hi:[1,0] neg_lo:[0,1] neg_hi:[0,1]
	v_pk_add_f32 v[116:117], v[116:117], v[184:185] op_sel_hi:[1,0] neg_lo:[0,1] neg_hi:[0,1]

.LBB0_2044:
	v_max3_f32 v98, v50, v51, v66
	v_max_f32_e32 v120, v65, v65
	v_max3_f32 v98, v98, v67, v52
	s_nop 0
	v_dot2c_f32_bf16 v34, 0x3f803f80, v94
	v_dot2c_f32_bf16 v35, 0x3f803f80, v95
	v_dot2c_f32_bf16 v34, 0x3f803f80, v96
	v_dot2c_f32_bf16 v35, 0x3f803f80, v97
	v_max3_f32 v98, v98, v68, v69
	v_max3_f32 v98, v98, v53, v54
	v_max3_f32 v98, v98, v70, v71
	v_max3_f32 v98, v98, v55, v56
	v_dot2c_f32_bf16 v34, 0x3f803f80, v100
	v_dot2c_f32_bf16 v35, 0x3f803f80, v101
	v_dot2c_f32_bf16 v34, 0x3f803f80, v102
	v_dot2c_f32_bf16 v35, 0x3f803f80, v103
	v_max3_f32 v98, v98, v72, v73
	v_max3_f32 v98, v98, v57, v58
	v_max3_f32 v98, v98, v74, v75
	v_max3_f32 v98, v98, v59, v60
	v_dot2c_f32_bf16 v34, 0x3f803f80, v90
	v_dot2c_f32_bf16 v35, 0x3f803f80, v91
	v_dot2c_f32_bf16 v34, 0x3f803f80, v92
	v_dot2c_f32_bf16 v35, 0x3f803f80, v93
	v_max3_f32 v98, v98, v76, v77
	v_max3_f32 v98, v98, v61, v62
	v_max3_f32 v98, v98, v78, v79
	v_max3_f32 v98, v98, v63, v64
	v_dot2c_f32_bf16 v34, 0x3f803f80, v86
	v_dot2c_f32_bf16 v35, 0x3f803f80, v87
	v_dot2c_f32_bf16 v34, 0x3f803f80, v88
	v_dot2c_f32_bf16 v35, 0x3f803f80, v89
	v_max3_f32 v98, v98, v80, v81
	v_max_f32_e32 v98, v98, v98
	v_max_f32_e32 v98, v98, v120
	v_mov_b32_e32 v120, v98
	s_nop 1
	v_permlane32_swap_b32_e32 v98, v120
	v_sub_f32_e32 v120, v98, v184
	s_waitcnt lgkmcnt(0)
	s_nop 0
	v_mfma_f32_32x32x16_bf16 v[18:33], v[116:119], v[94:97], v[18:33]
	v_mfma_f32_32x32x16_bf16 v[2:17], v[112:115], v[94:97], v[2:17]
	ds_read_b64_tr_b16 v[94:95], v202 offset:4096
	ds_read_b64_tr_b16 v[96:97], v202 offset:5120
	v_mfma_f32_32x32x16_bf16 v[18:33], v[108:111], v[100:103], v[18:33]
	v_mfma_f32_32x32x16_bf16 v[2:17], v[104:107], v[100:103], v[2:17]
	ds_read_b64_tr_b16 v[100:101], v203 offset:4096
	ds_read_b64_tr_b16 v[102:103], v203 offset:5120
	ds_read_b64_tr_b16 v[104:105], v202 offset:6144
	ds_read_b64_tr_b16 v[106:107], v202 offset:7168
	ds_read_b64_tr_b16 v[108:109], v203 offset:6144
	ds_read_b64_tr_b16 v[110:111], v203 offset:7168
	s_nop 0
	s_waitcnt lgkmcnt(0)
	s_nop 0
	v_mfma_f32_32x32x16_bf16 v[18:33], v[94:97], v[90:93], v[18:33]
	v_mfma_f32_32x32x16_bf16 v[2:17], v[100:103], v[90:93], v[2:17]
	v_mfma_f32_32x32x16_bf16 v[18:33], v[104:107], v[86:89], v[18:33]
	v_mfma_f32_32x32x16_bf16 v[2:17], v[108:111], v[86:89], v[2:17]
	v_cmp_lt_f32_e32 vcc, s29, v120
	s_cbranch_vccz .LBB0_2046
	v_max_f32_e32 v86, v120, v120
	v_max_f32_e32 v87, 0, v86
	v_exp_f32_e64 v86, -v87
	v_add_f32_e32 v184, v184, v87
	v_mul_f32_e32 v175, v175, v86
	v_pk_mul_f32 v[48:49], v[48:49], v[86:87] op_sel_hi:[1,0]
	v_pk_mul_f32 v[46:47], v[46:47], v[86:87] op_sel_hi:[1,0]
	v_pk_mul_f32 v[44:45], v[44:45], v[86:87] op_sel_hi:[1,0]
	v_pk_mul_f32 v[42:43], v[42:43], v[86:87] op_sel_hi:[1,0]
	v_pk_mul_f32 v[40:41], v[40:41], v[86:87] op_sel_hi:[1,0]
	v_pk_mul_f32 v[38:39], v[38:39], v[86:87] op_sel_hi:[1,0]
	v_pk_mul_f32 v[36:37], v[36:37], v[86:87] op_sel_hi:[1,0]
	v_pk_mul_f32 v[34:35], v[34:35], v[86:87] op_sel_hi:[1,0]
	v_pk_mul_f32 v[16:17], v[86:87], v[16:17] op_sel_hi:[0,1]
	v_pk_mul_f32 v[14:15], v[86:87], v[14:15] op_sel_hi:[0,1]
	v_pk_mul_f32 v[12:13], v[86:87], v[12:13] op_sel_hi:[0,1]
	v_pk_mul_f32 v[10:11], v[86:87], v[10:11] op_sel_hi:[0,1]
	v_pk_mul_f32 v[8:9], v[86:87], v[8:9] op_sel_hi:[0,1]
	v_pk_mul_f32 v[6:7], v[86:87], v[6:7] op_sel_hi:[0,1]
	v_pk_mul_f32 v[4:5], v[86:87], v[4:5] op_sel_hi:[0,1]
	v_pk_mul_f32 v[2:3], v[86:87], v[2:3] op_sel_hi:[0,1]
	v_pk_mul_f32 v[32:33], v[86:87], v[32:33] op_sel_hi:[0,1]
	v_pk_mul_f32 v[30:31], v[86:87], v[30:31] op_sel_hi:[0,1]
	v_pk_mul_f32 v[28:29], v[86:87], v[28:29] op_sel_hi:[0,1]
	v_pk_mul_f32 v[26:27], v[86:87], v[26:27] op_sel_hi:[0,1]
	v_pk_mul_f32 v[24:25], v[86:87], v[24:25] op_sel_hi:[0,1]
	v_pk_mul_f32 v[22:23], v[86:87], v[22:23] op_sel_hi:[0,1]
	v_pk_mul_f32 v[20:21], v[86:87], v[20:21] op_sel_hi:[0,1]
	v_pk_mul_f32 v[18:19], v[86:87], v[18:19] op_sel_hi:[0,1]
.LBB0_2046:
	v_cmp_neq_f32_e32 vcc, 0, v184
	s_cbranch_vccz .LBB0_2048
	v_pk_add_f32 v[64:65], v[64:65], v[184:185] op_sel_hi:[1,0] neg_lo:[0,1] neg_hi:[0,1]
	v_pk_add_f32 v[62:63], v[62:63], v[184:185] op_sel_hi:[1,0] neg_lo:[0,1] neg_hi:[0,1]
	v_pk_add_f32 v[60:61], v[60:61], v[184:185] op_sel_hi:[1,0] neg_lo:[0,1] neg_hi:[0,1]
	v_pk_add_f32 v[58:59], v[58:59], v[184:185] op_sel_hi:[1,0] neg_lo:[0,1] neg_hi:[0,1]
	v_pk_add_f32 v[56:57], v[56:57], v[184:185] op_sel_hi:[1,0] neg_lo:[0,1] neg_hi:[0,1]
	v_pk_add_f32 v[54:55], v[54:55], v[184:185] op_sel_hi:[1,0] neg_lo:[0,1] neg_hi:[0,1]
	v_pk_add_f32 v[52:53], v[52:53], v[184:185] op_sel_hi:[1,0] neg_lo:[0,1] neg_hi:[0,1]
	v_pk_add_f32 v[50:51], v[50:51], v[184:185] op_sel_hi:[1,0] neg_lo:[0,1] neg_hi:[0,1]
	v_pk_add_f32 v[80:81], v[80:81], v[184:185] op_sel_hi:[1,0] neg_lo:[0,1] neg_hi:[0,1]
	v_pk_add_f32 v[78:79], v[78:79], v[184:185] op_sel_hi:[1,0] neg_lo:[0,1] neg_hi:[0,1]
	v_pk_add_f32 v[76:77], v[76:77], v[184:185] op_sel_hi:[1,0] neg_lo:[0,1] neg_hi:[0,1]
	v_pk_add_f32 v[74:75], v[74:75], v[184:185] op_sel_hi:[1,0] neg_lo:[0,1] neg_hi:[0,1]
	v_pk_add_f32 v[72:73], v[72:73], v[184:185] op_sel_hi:[1,0] neg_lo:[0,1] neg_hi:[0,1]
	v_pk_add_f32 v[70:71], v[70:71], v[184:185] op_sel_hi:[1,0] neg_lo:[0,1] neg_hi:[0,1]
	v_pk_add_f32 v[68:69], v[68:69], v[184:185] op_sel_hi:[1,0] neg_lo:[0,1] neg_hi:[0,1]
	v_pk_add_f32 v[66:67], v[66:67], v[184:185] op_sel_hi:[1,0] neg_lo:[0,1] neg_hi:[0,1]

.LBB0_2087:
	v_mov_b64_e32 v[124:125], s[94:95]
	v_mov_b64_e32 v[122:123], s[92:93]
	v_max3_f32 v118, v50, v51, v66
	v_max_f32_e32 v119, v65, v65
	v_max3_f32 v118, v118, v67, v52
	s_nop 0
	v_dot2c_f32_bf16 v34, 0x3f803f80, v108
	v_dot2c_f32_bf16 v35, 0x3f803f80, v109
	v_dot2c_f32_bf16 v34, 0x3f803f80, v110
	v_dot2c_f32_bf16 v35, 0x3f803f80, v111
	v_max3_f32 v118, v118, v68, v69
	s_nop 0
	v_max3_f32 v118, v118, v53, v54
	s_nop 0
	v_max3_f32 v118, v118, v70, v71
	s_nop 0
	v_max3_f32 v118, v118, v55, v56
	v_dot2c_f32_bf16 v34, 0x3f803f80, v112
	v_dot2c_f32_bf16 v35, 0x3f803f80, v113
	v_dot2c_f32_bf16 v34, 0x3f803f80, v114
	v_dot2c_f32_bf16 v35, 0x3f803f80, v115
	v_max3_f32 v118, v118, v72, v73
	s_nop 0
	v_max3_f32 v118, v118, v57, v58
	s_nop 0
	v_max3_f32 v118, v118, v74, v75
	s_nop 0
	v_max3_f32 v118, v118, v59, v60
	v_dot2c_f32_bf16 v34, 0x3f803f80, v104
	v_dot2c_f32_bf16 v35, 0x3f803f80, v105
	v_dot2c_f32_bf16 v34, 0x3f803f80, v106
	v_dot2c_f32_bf16 v35, 0x3f803f80, v107
	v_max3_f32 v118, v118, v76, v77
	s_nop 0
	v_max3_f32 v118, v118, v61, v62
	s_nop 0
	v_max3_f32 v118, v118, v78, v79
	s_nop 0
	v_max3_f32 v118, v118, v63, v64
	v_dot2c_f32_bf16 v34, 0x3f803f80, v100
	v_dot2c_f32_bf16 v35, 0x3f803f80, v101
	v_dot2c_f32_bf16 v34, 0x3f803f80, v102
	v_dot2c_f32_bf16 v35, 0x3f803f80, v103
	v_max3_f32 v118, v118, v80, v81
	s_nop 0
	v_max_f32_e32 v118, v118, v118
	v_max_f32_e32 v118, v118, v119
	v_mov_b32_e32 v119, v118
	s_nop 1
	v_permlane32_swap_b32_e32 v118, v119
	v_sub_f32_e32 v120, v118, v184
	s_waitcnt lgkmcnt(0)
	s_nop 0
	v_mfma_f32_32x32x16_bf16 v[18:33], v[94:97], v[108:111], v[18:33]
	v_mfma_f32_32x32x16_bf16 v[2:17], v[90:93], v[108:111], v[2:17]
	v_mfma_f32_32x32x16_bf16 v[18:33], v[86:89], v[112:115], v[18:33]
	v_mfma_f32_32x32x16_bf16 v[2:17], v[82:85], v[112:115], v[2:17]
	ds_read_b64_tr_b16 v[82:83], v117 offset:4096
	ds_read_b64_tr_b16 v[84:85], v117 offset:5120
	ds_read_b64_tr_b16 v[86:87], v98 offset:4096
	ds_read_b64_tr_b16 v[88:89], v98 offset:5120
	ds_read_b64_tr_b16 v[90:91], v117 offset:6144
	ds_read_b64_tr_b16 v[92:93], v117 offset:7168
	ds_read_b64_tr_b16 v[94:95], v98 offset:6144
	ds_read_b64_tr_b16 v[96:97], v98 offset:7168
	s_nop 0
	s_waitcnt lgkmcnt(0)
	s_nop 0
	v_mfma_f32_32x32x16_bf16 v[18:33], v[82:85], v[104:107], v[18:33]
	v_mfma_f32_32x32x16_bf16 v[2:17], v[86:89], v[104:107], v[2:17]
	v_mfma_f32_32x32x16_bf16 v[18:33], v[90:93], v[100:103], v[18:33]
	v_mfma_f32_32x32x16_bf16 v[2:17], v[94:97], v[100:103], v[2:17]
	v_cmp_lt_f32_e32 vcc, s29, v120
	s_cbranch_vccz .LBB0_2089
	v_max_f32_e32 v82, v120, v120
	v_max_f32_e32 v83, 0, v82
	v_exp_f32_e64 v82, -v83
	v_add_f32_e32 v184, v184, v83
	v_mul_f32_e32 v175, v175, v82
	v_pk_mul_f32 v[48:49], v[48:49], v[82:83] op_sel_hi:[1,0]
	v_pk_mul_f32 v[46:47], v[46:47], v[82:83] op_sel_hi:[1,0]
	v_pk_mul_f32 v[44:45], v[44:45], v[82:83] op_sel_hi:[1,0]
	v_pk_mul_f32 v[42:43], v[42:43], v[82:83] op_sel_hi:[1,0]
	v_pk_mul_f32 v[40:41], v[40:41], v[82:83] op_sel_hi:[1,0]
	v_pk_mul_f32 v[38:39], v[38:39], v[82:83] op_sel_hi:[1,0]
	v_pk_mul_f32 v[36:37], v[36:37], v[82:83] op_sel_hi:[1,0]
	v_pk_mul_f32 v[34:35], v[34:35], v[82:83] op_sel_hi:[1,0]
	v_pk_mul_f32 v[16:17], v[82:83], v[16:17] op_sel_hi:[0,1]
	v_pk_mul_f32 v[14:15], v[82:83], v[14:15] op_sel_hi:[0,1]
	v_pk_mul_f32 v[12:13], v[82:83], v[12:13] op_sel_hi:[0,1]
	v_pk_mul_f32 v[10:11], v[82:83], v[10:11] op_sel_hi:[0,1]
	v_pk_mul_f32 v[8:9], v[82:83], v[8:9] op_sel_hi:[0,1]
	v_pk_mul_f32 v[6:7], v[82:83], v[6:7] op_sel_hi:[0,1]
	v_pk_mul_f32 v[4:5], v[82:83], v[4:5] op_sel_hi:[0,1]
	v_pk_mul_f32 v[2:3], v[82:83], v[2:3] op_sel_hi:[0,1]
	v_pk_mul_f32 v[32:33], v[82:83], v[32:33] op_sel_hi:[0,1]
	v_pk_mul_f32 v[30:31], v[82:83], v[30:31] op_sel_hi:[0,1]
	v_pk_mul_f32 v[28:29], v[82:83], v[28:29] op_sel_hi:[0,1]
	v_pk_mul_f32 v[26:27], v[82:83], v[26:27] op_sel_hi:[0,1]
	v_pk_mul_f32 v[24:25], v[82:83], v[24:25] op_sel_hi:[0,1]
	v_pk_mul_f32 v[22:23], v[82:83], v[22:23] op_sel_hi:[0,1]
	v_pk_mul_f32 v[20:21], v[82:83], v[20:21] op_sel_hi:[0,1]
	v_pk_mul_f32 v[18:19], v[82:83], v[18:19] op_sel_hi:[0,1]
